# expert weight conversion of layers 1-3 out of the prologue into barrier waits; early-workgroup thresholds made conservative against routing skew
# baseline (speedup 1.0000x reference)
.Lcvt_sx0:
	s_cmp_eq_u32 s31, 10
	s_cbranch_scc0 .Lcvt_sx1
	s_cmp_ge_u32 s62, 3
	s_cbranch_scc1 .Lcvt_ret
	s_sub_i32 s27, s63, 136
	s_cmp_lt_i32 s27, 0
	s_cbranch_scc1 .Lcvt_ret
	s_mov_b32 s26, 4
	s_movk_i32 s30, 5040
	s_branch .Lcvt_go
.Lcvt_sx1:
	s_cmp_eq_u32 s31, 3
	s_cbranch_scc0 .Lcvt_sx2
	s_cmp_ge_u32 s62, 3
	s_cbranch_scc1 .Lcvt_ret
	s_sub_i32 s27, s63, 208
	s_cmp_lt_i32 s27, 0
	s_cbranch_scc1 .Lcvt_ret
	s_mov_b32 s26, 1
	s_movk_i32 s30, 8400
	s_branch .Lcvt_go
.Lcvt_sx2:
	s_mov_b32 s27, -1
	s_cmp_eq_u32 s31, 0
	s_cselect_b32 s27, 0, s27
	s_cmp_eq_u32 s31, 1
	s_cselect_b32 s27, 1, s27
	s_cmp_eq_u32 s31, 2
	s_cselect_b32 s27, 2, s27
	s_cmp_eq_u32 s31, 4
	s_cselect_b32 s27, 3, s27
	s_cmp_eq_u32 s31, 6
	s_cselect_b32 s27, 4, s27
	s_cmp_eq_u32 s31, 7
	s_cselect_b32 s27, 5, s27
	s_cmp_eq_u32 s31, 8
	s_cselect_b32 s27, 6, s27
	s_cmp_eq_u32 s31, 9
	s_cselect_b32 s27, 7, s27
	s_cmp_lt_i32 s27, 0
	s_cbranch_scc1 .Lcvt_ret
	s_mul_i32 s26, s62, 8
	s_add_i32 s27, s27, s26
	s_mul_i32 s27, s27, 0x700
	s_mul_i32 s26, s80, 7
	s_add_i32 s27, s27, s26
	s_add_i32 s27, s27, s25
	s_add_i32 s27, s27, -1
	s_cmp_ge_u32 s27, 47520
	s_cbranch_scc1 .Lcvt_ret
	s_mov_b32 s26, 1
	s_cmp_ge_u32 s27, 15840
	s_cbranch_scc0 .Lcvt_lk
	s_sub_i32 s27, s27, 15840
	s_mov_b32 s26, 2
	s_cmp_ge_u32 s27, 15840
	s_cbranch_scc0 .Lcvt_lk
	s_sub_i32 s27, s27, 15840
	s_mov_b32 s26, 3
.Lcvt_lk:
	s_add_i32 s30, s27, 8736
	s_mov_b32 s27, s26
	s_mov_b32 s26, 1
	s_movk_i32 s4, 0x6000
	s_branch .Lcvt_lanes
.Lcvt_go:
	s_mul_i32 s27, s27, 7
	s_add_i32 s27, s27, s25
	s_add_i32 s27, s27, -1
	s_mul_i32 s27, s27, s26
	s_add_i32 s30, s30, s27
	s_add_i32 s27, s62, 1
	s_movk_i32 s4, 8736
